# ticket order: conversion chunks dealt 20% behind the attention work (a fifth of the chunks left for the end)
# baseline (speedup 1.0000x reference)
_ZN3attL9ATT_ORDERE:
	.short	8207
	.short	8206
	.short	8205
	.short	8204
	.short	8203
	.short	8202
	.short	8201
	.short	8200
	.short	8199
	.short	8198
	.short	8197
	.short	8196
	.short	8195
	.short	8194
	.short	8193
	.short	8271
	.short	8270
	.short	8269
	.short	8268
	.short	8267
	.short	8266
	.short	8265
	.short	8264
	.short	8263
	.short	8262
	.short	8261
	.short	8260
	.short	8259
	.short	8258
	.short	8257
	.short	8335
	.short	8334
	.short	8333
	.short	8332
	.short	8331
	.short	8330
	.short	8329
	.short	8328
	.short	8327
	.short	8326
	.short	8325
	.short	8324
	.short	8323
	.short	8322
	.short	8321
	.short	8399
	.short	8398
	.short	8397
	.short	8396
	.short	8395
	.short	8394
	.short	8393
	.short	8392
	.short	8391
	.short	8390
	.short	8389
	.short	8388
	.short	8387
	.short	8386
	.short	8385
	.short	8463
	.short	8462
	.short	8461
	.short	8460
	.short	8459
	.short	8458
	.short	8457
	.short	8456
	.short	8455
	.short	8454
	.short	8453
	.short	8452
	.short	8451
	.short	8450
	.short	8449
	.short	8719
	.short	8718
	.short	8717
	.short	8716
	.short	8715
	.short	8714
	.short	8713
	.short	8712
	.short	8711
	.short	8710
	.short	8709
	.short	8708
	.short	8707
	.short	8706
	.short	8705
	.short	8783
	.short	8782
	.short	8781
	.short	8780
	.short	8779
	.short	8778
	.short	8777
	.short	8776
	.short	8775
	.short	8774
	.short	8773
	.short	8772
	.short	8771
	.short	8770
	.short	8769
	.short	8847
	.short	8846
	.short	8845
	.short	8844
	.short	8843
	.short	8842
	.short	8841
	.short	8840
	.short	8839
	.short	8838
	.short	8837
	.short	8836
	.short	8835
	.short	8834
	.short	8833
	.short	8911
	.short	8910
	.short	8909
	.short	8908
	.short	8907
	.short	8906
	.short	8905
	.short	8904
	.short	8903
	.short	8902
	.short	8901
	.short	8900
	.short	8899
	.short	8898
	.short	8897
	.short	8975
	.short	8974
	.short	8973
	.short	8972
	.short	8971
	.short	8970
	.short	8969
	.short	8968
	.short	8967
	.short	8966
	.short	8965
	.short	8964
	.short	8963
	.short	8962
	.short	8961
	.short	2063
	.short	32768
	.short	2127
	.short	32769
	.short	32770
	.short	2191
	.short	32771
	.short	32772
	.short	2255
	.short	32773
	.short	2319
	.short	32774
	.short	32775
	.short	2575
	.short	32776
	.short	32777
	.short	2639
	.short	32778
	.short	32779
	.short	2703
	.short	32780
	.short	2767
	.short	32781
	.short	32782
	.short	2831
	.short	32783
	.short	32784
	.short	2062
	.short	32785
	.short	2126
	.short	32786
	.short	32787
	.short	2190
	.short	32788
	.short	32789
	.short	2254
	.short	32790
	.short	32791
	.short	2318
	.short	32792
	.short	2574
	.short	32793
	.short	32794
	.short	2638
	.short	32795
	.short	32796
	.short	2702
	.short	32797
	.short	32798
	.short	2766
	.short	32799
	.short	2830
	.short	32800
	.short	32801
	.short	2061
	.short	32802
	.short	32803
	.short	2125
	.short	32804
	.short	2189
	.short	32805
	.short	32806
	.short	2253
	.short	32807
	.short	32808
	.short	2317
	.short	32809
	.short	32810
	.short	2573
	.short	32811
	.short	2637
	.short	32812
	.short	32813
	.short	2701
	.short	32814
	.short	32815
	.short	2765
	.short	32816
	.short	2829
	.short	32817
	.short	32818
	.short	2060
	.short	32819
	.short	32820
	.short	2124
	.short	32821
	.short	32822
	.short	2188
	.short	32823
	.short	2252
	.short	32824
	.short	32825
	.short	2316
	.short	32826
	.short	32827
	.short	2572
	.short	32828
	.short	32829
	.short	2636
	.short	32830
	.short	2700
	.short	32831
	.short	32832
	.short	2764
	.short	32833
	.short	32834
	.short	2828
	.short	32835
	.short	2059
	.short	32836
	.short	32837
	.short	2123
	.short	32838
	.short	32839
	.short	2187
	.short	32840
	.short	32841
	.short	2251
	.short	32842
	.short	2315
	.short	32843
	.short	32844
	.short	2571
	.short	32845
	.short	32846
	.short	2635
	.short	32847
	.short	2699
	.short	32848
	.short	32849
	.short	2763
	.short	32850
	.short	32851
	.short	2827
	.short	32852
	.short	32853
	.short	2058
	.short	32854
	.short	2122
	.short	32855
	.short	32856
	.short	2186
	.short	32857
	.short	32858
	.short	2250
	.short	32859
	.short	32860
	.short	2314
	.short	32861
	.short	2570
	.short	32862
	.short	32863
	.short	2634
	.short	32864
	.short	32865
	.short	2698
	.short	32866
	.short	2762
	.short	32867
	.short	32868
	.short	2826
	.short	32869
	.short	32870
	.short	2057
	.short	32871
	.short	32872
	.short	2121
	.short	32873
	.short	2185
	.short	32874
	.short	32875
	.short	2249
	.short	32876
	.short	32877
	.short	2313
	.short	32878
	.short	2569
	.short	32879
	.short	32880
	.short	2633
	.short	32881
	.short	32882
	.short	2697
	.short	32883
	.short	32884
	.short	2761
	.short	32885
	.short	2825
	.short	32886
	.short	32887
	.short	2056
	.short	32888
	.short	32889
	.short	2120
	.short	32890
	.short	32891
	.short	2184
	.short	32892
	.short	2248
	.short	32893
	.short	32894
	.short	2312
	.short	32895
	.short	32896
	.short	2568
	.short	32897
	.short	2632
	.short	32898
	.short	32899
	.short	2696
	.short	32900
	.short	32901
	.short	2760
	.short	32902
	.short	32903
	.short	2824
	.short	32904
	.short	2055
	.short	32905
	.short	32906
	.short	2119
	.short	32907
	.short	32908
	.short	2183
	.short	32909
	.short	32910
	.short	2247
	.short	32911
	.short	2311
	.short	32912
	.short	32913
	.short	2567
	.short	32914
	.short	32915
	.short	2631
	.short	32916
	.short	2695
	.short	32917
	.short	32918
	.short	2759
	.short	32919
	.short	32920
	.short	2823
	.short	32921
	.short	32922
	.short	2054
	.short	32923
	.short	2118
	.short	32924
	.short	32925
	.short	2182
	.short	32926
	.short	32927
	.short	2246
	.short	32928
	.short	2310
	.short	32929
	.short	32930
	.short	2566
	.short	32931
	.short	32932
	.short	2630
	.short	32933
	.short	32934
	.short	2694
	.short	32935
	.short	2758
	.short	32936
	.short	32937
	.short	2822
	.short	32938
	.short	32939
	.short	2053
	.short	32940
	.short	32941
	.short	2117
	.short	32942
	.short	2181
	.short	32943
	.short	32944
	.short	2245
	.short	32945
	.short	32946
	.short	2309
	.short	32947
	.short	2565
	.short	32948
	.short	32949
	.short	2629
	.short	32950
	.short	32951
	.short	2693
	.short	32952
	.short	32953
	.short	2757
	.short	32954
	.short	2821
	.short	32955
	.short	32956
	.short	2052
	.short	32957
	.short	32958
	.short	2116
	.short	32959
	.short	2180
	.short	32960
	.short	32961
	.short	2244
	.short	32962
	.short	32963
	.short	2308
	.short	32964
	.short	32965
	.short	2564
	.short	32966
	.short	2628
	.short	32967
	.short	32968
	.short	2692
	.short	32969
	.short	32970
	.short	2756
	.short	32971
	.short	32972
	.short	2820
	.short	32973
	.short	2051
	.short	32974
	.short	32975
	.short	2115
	.short	32976
	.short	32977
	.short	2179
	.short	32978
	.short	2243
	.short	32979
	.short	32980
	.short	2307
	.short	32981
	.short	32982
	.short	2563
	.short	32983
	.short	32984
	.short	2627
	.short	32985
	.short	2691
	.short	32986
	.short	32987
	.short	2755
	.short	32988
	.short	32989
	.short	2819
	.short	32990
	.short	2050
	.short	32991
	.short	32992
	.short	2114
	.short	32993
	.short	32994
	.short	2178
	.short	32995
	.short	32996
	.short	2242
	.short	32997
	.short	2306
	.short	32998
	.short	32999
	.short	2562
	.short	33000
	.short	33001
	.short	2626
	.short	33002
	.short	33003
	.short	2690
	.short	33004
	.short	2754
	.short	33005
	.short	33006
	.short	2818
	.short	33007
	.short	33008
	.short	2049
	.short	33009
	.short	2113
	.short	33010
	.short	33011
	.short	2177
	.short	33012
	.short	33013
	.short	2241
	.short	33014
	.short	33015
	.short	2305
	.short	33016
	.short	2561
	.short	33017
	.short	33018
	.short	2625
	.short	33019
	.short	33020
	.short	2689
	.short	33021
	.short	2753
	.short	33022
	.short	33023
	.short	2817
	.short	33024
	.short	33025
	.short	2048
	.short	33026
	.short	2112
	.short	33027
	.short	2176
	.short	33028
	.short	2240
	.short	33029
	.short	33030
	.short	2304
	.short	33031
	.short	2560
	.short	33032
	.short	2624
	.short	33033
	.short	2688
	.short	33034
	.short	2752
	.short	33035
	.short	2816
	.short	33036
	.short	1039
	.short	33037
	.short	33038
	.short	1103
	.short	33039
	.short	1167
	.short	33040
	.short	1231
	.short	33041
	.short	1295
	.short	33042
	.short	1551
	.short	33043
	.short	1615
	.short	33044
	.short	1679
	.short	33045
	.short	33046
	.short	1743
	.short	33047
	.short	1807
	.short	33048
	.short	1038
	.short	33049
	.short	1102
	.short	33050
	.short	1166
	.short	33051
	.short	1230
	.short	33052
	.short	33053
	.short	1294
	.short	33054
	.short	1550
	.short	33055
	.short	1614
	.short	33056
	.short	1678
	.short	33057
	.short	1742
	.short	33058
	.short	1806
	.short	33059
	.short	1037
	.short	33060
	.short	33061
	.short	1101
	.short	33062
	.short	1165
	.short	33063
	.short	1229
	.short	33064
	.short	1293
	.short	33065
	.short	1549
	.short	33066
	.short	1613
	.short	33067
	.short	1677
	.short	33068
	.short	33069
	.short	1741
	.short	33070
	.short	1805
	.short	33071
	.short	1036
	.short	33072
	.short	1100
	.short	33073
	.short	1164
	.short	33074
	.short	1228
	.short	33075
	.short	1292
	.short	33076
	.short	33077
	.short	1548
	.short	33078
	.short	1612
	.short	33079
	.short	1676
	.short	33080
	.short	1740
	.short	33081
	.short	1804
	.short	33082
	.short	1035
	.short	33083
	.short	33084
	.short	1099
	.short	33085
	.short	1163
	.short	33086
	.short	1227
	.short	33087
	.short	1291
	.short	33088
	.short	1547
	.short	33089
	.short	1611
	.short	33090
	.short	1675
	.short	33091
	.short	33092
	.short	1739
	.short	33093
	.short	1803
	.short	33094
	.short	1034
	.short	33095
	.short	1098
	.short	33096
	.short	1162
	.short	33097
	.short	1226
	.short	33098
	.short	1290
	.short	33099
	.short	33100
	.short	1546
	.short	33101
	.short	1610
	.short	33102
	.short	1674
	.short	33103
	.short	1738
	.short	33104
	.short	1802
	.short	33105
	.short	1033
	.short	33106
	.short	1097
	.short	33107
	.short	33108
	.short	1161
	.short	33109
	.short	1225
	.short	33110
	.short	1289
	.short	33111
	.short	1545
	.short	33112
	.short	1609
	.short	33113
	.short	1673
	.short	33114
	.short	33115
	.short	1737
	.short	33116
	.short	1801
	.short	33117
	.short	1032
	.short	33118
	.short	1096
	.short	33119
	.short	1160
	.short	33120
	.short	1224
	.short	33121
	.short	1288
	.short	33122
	.short	33123
	.short	1544
	.short	33124
	.short	1608
	.short	33125
	.short	1672
	.short	33126
	.short	1736
	.short	33127
	.short	1800
	.short	33128
	.short	1031
	.short	33129
	.short	1095
	.short	33130
	.short	33131
	.short	1159
	.short	33132
	.short	1223
	.short	33133
	.short	1287
	.short	33134
	.short	1543
	.short	33135
	.short	1607
	.short	33136
	.short	1671
	.short	33137
	.short	1735
	.short	33138
	.short	33139
	.short	1799
	.short	33140
	.short	1030
	.short	33141
	.short	1094
	.short	33142
	.short	1158
	.short	33143
	.short	1222
	.short	33144
	.short	1286
	.short	33145
	.short	33146
	.short	1542
	.short	33147
	.short	1606
	.short	33148
	.short	1670
	.short	33149
	.short	1734
	.short	33150
	.short	1798
	.short	33151
	.short	1029
	.short	33152
	.short	1093
	.short	33153
	.short	33154
	.short	1157
	.short	33155
	.short	1221
	.short	33156
	.short	1285
	.short	33157
	.short	1541
	.short	33158
	.short	1605
	.short	33159
	.short	1669
	.short	33160
	.short	1733
	.short	33161
	.short	33162
	.short	1797
	.short	33163
	.short	1028
	.short	33164
	.short	1092
	.short	33165
	.short	1156
	.short	33166
	.short	1220
	.short	33167
	.short	1284
	.short	33168
	.short	33169
	.short	1540
	.short	33170
	.short	1604
	.short	33171
	.short	1668
	.short	33172
	.short	1732
	.short	33173
	.short	1796
	.short	33174
	.short	1027
	.short	33175
	.short	1091
	.short	33176
	.short	33177
	.short	1155
	.short	33178
	.short	1219
	.short	33179
	.short	1283
	.short	33180
	.short	1539
	.short	33181
	.short	1603
	.short	33182
	.short	1667
	.short	33183
	.short	1731
	.short	33184
	.short	33185
	.short	1795
	.short	33186
	.short	1026
	.short	33187
	.short	1090
	.short	33188
	.short	1154
	.short	33189
	.short	1218
	.short	33190
	.short	1282
	.short	33191
	.short	1538
	.short	33192
	.short	33193
	.short	1602
	.short	33194
	.short	1666
	.short	33195
	.short	1730
	.short	33196
	.short	1794
	.short	33197
	.short	1025
	.short	33198
	.short	1089
	.short	33199
	.short	33200
	.short	1153
	.short	33201
	.short	1217
	.short	33202
	.short	1281
	.short	33203
	.short	1537
	.short	33204
	.short	1601
	.short	33205
	.short	1665
	.short	33206
	.short	1729
	.short	33207
	.short	33208
	.short	1793
	.short	33209
	.short	1024
	.short	33210
	.short	1088
	.short	33211
	.short	1152
	.short	33212
	.short	1216
	.short	33213
	.short	1280
	.short	33214
	.short	1536
	.short	33215
	.short	33216
	.short	1600
	.short	33217
	.short	1664
	.short	33218
	.short	1728
	.short	33219
	.short	1792
	.short	33220
	.short	47
	.short	33221
	.short	111
	.short	33222
	.short	175
	.short	33223
	.short	33224
	.short	239
	.short	33225
	.short	303
	.short	33226
	.short	367
	.short	33227
	.short	559
	.short	33228
	.short	623
	.short	33229
	.short	687
	.short	33230
	.short	33231
	.short	751
	.short	33232
	.short	815
	.short	33233
	.short	879
	.short	33234
	.short	46
	.short	33235
	.short	110
	.short	33236
	.short	174
	.short	33237
	.short	238
	.short	33238
	.short	33239
	.short	302
	.short	33240
	.short	366
	.short	33241
	.short	558
	.short	33242
	.short	622
	.short	33243
	.short	686
	.short	33244
	.short	750
	.short	33245
	.short	814
	.short	33246
	.short	33247
	.short	878
	.short	33248
	.short	45
	.short	33249
	.short	109
	.short	33250
	.short	173
	.short	33251
	.short	237
	.short	33252
	.short	301
	.short	33253
	.short	33254
	.short	365
	.short	33255
	.short	557
	.short	33256
	.short	621
	.short	33257
	.short	685
	.short	33258
	.short	749
	.short	33259
	.short	813
	.short	33260
	.short	877
	.short	33261
	.short	33262
	.short	44
	.short	33263
	.short	108
	.short	33264
	.short	172
	.short	33265
	.short	236
	.short	33266
	.short	300
	.short	33267
	.short	364
	.short	33268
	.short	556
	.short	33269
	.short	33270
	.short	620
	.short	33271
	.short	684
	.short	33272
	.short	748
	.short	33273
	.short	812
	.short	33274
	.short	876
	.short	33275
	.short	43
	.short	33276
	.short	107
	.short	33277
	.short	33278
	.short	171
	.short	33279
	.short	235
	.short	33280
	.short	299
	.short	33281
	.short	363
	.short	33282
	.short	555
	.short	33283
	.short	619
	.short	33284
	.short	33285
	.short	683
	.short	33286
	.short	747
	.short	33287
	.short	811
	.short	33288
	.short	875
	.short	33289
	.short	42
	.short	33290
	.short	106
	.short	33291
	.short	170
	.short	33292
	.short	33293
	.short	234
	.short	33294
	.short	298
	.short	33295
	.short	362
	.short	33296
	.short	554
	.short	33297
	.short	618
	.short	33298
	.short	682
	.short	33299
	.short	746
	.short	33300
	.short	33301
	.short	810
	.short	33302
	.short	874
	.short	33303
	.short	41
	.short	33304
	.short	105
	.short	33305
	.short	169
	.short	33306
	.short	233
	.short	33307
	.short	297
	.short	33308
	.short	33309
	.short	361
	.short	33310
	.short	553
	.short	33311
	.short	617
	.short	33312
	.short	681
	.short	33313
	.short	745
	.short	33314
	.short	809
	.short	33315
	.short	33316
	.short	873
	.short	33317
	.short	40
	.short	33318
	.short	104
	.short	33319
	.short	168
	.short	33320
	.short	232
	.short	33321
	.short	296
	.short	33322
	.short	360
	.short	33323
	.short	33324
	.short	552
	.short	33325
	.short	616
	.short	33326
	.short	680
	.short	33327
	.short	744
	.short	33328
	.short	808
	.short	33329
	.short	872
	.short	33330
	.short	39
	.short	33331
	.short	33332
	.short	103
	.short	33333
	.short	167
	.short	33334
	.short	231
	.short	33335
	.short	295
	.short	33336
	.short	359
	.short	33337
	.short	551
	.short	33338
	.short	33339
	.short	615
	.short	33340
	.short	679
	.short	33341
	.short	743
	.short	33342
	.short	807
	.short	33343
	.short	871
	.short	33344
	.short	38
	.short	33345
	.short	102
	.short	33346
	.short	33347
	.short	166
	.short	33348
	.short	230
	.short	33349
	.short	294
	.short	33350
	.short	358
	.short	33351
	.short	550
	.short	33352
	.short	614
	.short	33353
	.short	678
	.short	33354
	.short	33355
	.short	742
	.short	33356
	.short	806
	.short	33357
	.short	870
	.short	33358
	.short	37
	.short	33359
	.short	101
	.short	33360
	.short	165
	.short	33361
	.short	229
	.short	33362
	.short	33363
	.short	293
	.short	33364
	.short	357
	.short	33365
	.short	549
	.short	33366
	.short	613
	.short	33367
	.short	677
	.short	33368
	.short	741
	.short	33369
	.short	33370
	.short	805
	.short	33371
	.short	869
	.short	33372
	.short	36
	.short	33373
	.short	100
	.short	33374
	.short	164
	.short	33375
	.short	228
	.short	33376
	.short	292
	.short	33377
	.short	33378
	.short	356
	.short	33379
	.short	548
	.short	33380
	.short	612
	.short	33381
	.short	676
	.short	33382
	.short	740
	.short	33383
	.short	804
	.short	33384
	.short	868
	.short	33385
	.short	33386
	.short	35
	.short	33387
	.short	99
	.short	33388
	.short	163
	.short	33389
	.short	227
	.short	33390
	.short	291
	.short	33391
	.short	355
	.short	33392
	.short	547
	.short	33393
	.short	33394
	.short	611
	.short	33395
	.short	675
	.short	33396
	.short	739
	.short	33397
	.short	803
	.short	33398
	.short	867
	.short	33399
	.short	34
	.short	33400
	.short	33401
	.short	98
	.short	33402
	.short	162
	.short	33403
	.short	226
	.short	33404
	.short	290
	.short	33405
	.short	354
	.short	33406
	.short	546
	.short	33407
	.short	610
	.short	33408
	.short	33409
	.short	674
	.short	33410
	.short	738
	.short	33411
	.short	802
	.short	33412
	.short	866
	.short	33413
	.short	33
	.short	33414
	.short	97
	.short	33415
	.short	161
	.short	33416
	.short	33417
	.short	225
	.short	33418
	.short	289
	.short	33419
	.short	353
	.short	33420
	.short	545
	.short	33421
	.short	609
	.short	33422
	.short	673
	.short	33423
	.short	33424
	.short	737
	.short	33425
	.short	801
	.short	33426
	.short	865
	.short	33427
	.short	32
	.short	33428
	.short	96
	.short	33429
	.short	160
	.short	33430
	.short	224
	.short	33431
	.short	33432
	.short	288
	.short	33433
	.short	352
	.short	33434
	.short	544
	.short	33435
	.short	608
	.short	33436
	.short	672
	.short	33437
	.short	736
	.short	33438
	.short	800
	.short	33439
	.short	33440
	.short	864
	.short	33441
	.short	31
	.short	33442
	.short	95
	.short	33443
	.short	159
	.short	33444
	.short	223
	.short	33445
	.short	287
	.short	33446
	.short	351
	.short	33447
	.short	33448
	.short	543
	.short	33449
	.short	607
	.short	33450
	.short	671
	.short	33451
	.short	735
	.short	33452
	.short	799
	.short	33453
	.short	863
	.short	33454
	.short	33455
	.short	30
	.short	33456
	.short	94
	.short	33457
	.short	158
	.short	33458
	.short	222
	.short	33459
	.short	286
	.short	33460
	.short	350
	.short	33461
	.short	542
	.short	33462
	.short	33463
	.short	606
	.short	33464
	.short	670
	.short	33465
	.short	734
	.short	33466
	.short	798
	.short	33467
	.short	862
	.short	33468
	.short	29
	.short	33469
	.short	93
	.short	33470
	.short	33471
	.short	157
	.short	33472
	.short	221
	.short	33473
	.short	285
	.short	33474
	.short	349
	.short	33475
	.short	541
	.short	33476
	.short	605
	.short	33477
	.short	669
	.short	33478
	.short	33479
	.short	733
	.short	33480
	.short	797
	.short	33481
	.short	861
	.short	33482
	.short	28
	.short	33483
	.short	92
	.short	33484
	.short	156
	.short	33485
	.short	33486
	.short	220
	.short	33487
	.short	284
	.short	33488
	.short	348
	.short	33489
	.short	540
	.short	33490
	.short	604
	.short	33491
	.short	668
	.short	33492
	.short	732
	.short	33493
	.short	33494
	.short	796
	.short	33495
	.short	860
	.short	33496
	.short	27
	.short	33497
	.short	91
	.short	33498
	.short	155
	.short	33499
	.short	219
	.short	33500
	.short	283
	.short	33501
	.short	33502
	.short	347
	.short	33503
	.short	539
	.short	33504
	.short	603
	.short	33505
	.short	667
	.short	33506
	.short	731
	.short	33507
	.short	795
	.short	33508
	.short	859
	.short	33509
	.short	33510
	.short	26
	.short	33511
	.short	90
	.short	33512
	.short	154
	.short	33513
	.short	218
	.short	33514
	.short	282
	.short	33515
	.short	346
	.short	33516
	.short	33517
	.short	538
	.short	33518
	.short	602
	.short	33519
	.short	666
	.short	33520
	.short	730
	.short	33521
	.short	794
	.short	33522
	.short	858
	.short	33523
	.short	25
	.short	33524
	.short	33525
	.short	89
	.short	33526
	.short	153
	.short	33527
	.short	217
	.short	33528
	.short	281
	.short	33529
	.short	345
	.short	33530
	.short	537
	.short	33531
	.short	601
	.short	33532
	.short	33533
	.short	665
	.short	33534
	.short	729
	.short	33535
	.short	793
	.short	33536
	.short	857
	.short	33537
	.short	24
	.short	33538
	.short	88
	.short	33539
	.short	33540
	.short	152
	.short	33541
	.short	216
	.short	33542
	.short	280
	.short	33543
	.short	344
	.short	33544
	.short	536
	.short	33545
	.short	600
	.short	33546
	.short	664
	.short	33547
	.short	33548
	.short	728
	.short	33549
	.short	792
	.short	33550
	.short	856
	.short	33551
	.short	23
	.short	33552
	.short	87
	.short	33553
	.short	151
	.short	33554
	.short	215
	.short	33555
	.short	33556
	.short	279
	.short	33557
	.short	343
	.short	33558
	.short	535
	.short	33559
	.short	599
	.short	33560
	.short	663
	.short	33561
	.short	727
	.short	33562
	.short	791
	.short	33563
	.short	33564
	.short	855
	.short	33565
	.short	22
	.short	33566
	.short	86
	.short	33567
	.short	150
	.short	33568
	.short	214
	.short	33569
	.short	278
	.short	33570
	.short	33571
	.short	342
	.short	33572
	.short	534
	.short	33573
	.short	598
	.short	33574
	.short	662
	.short	33575
	.short	726
	.short	33576
	.short	790
	.short	33577
	.short	854
	.short	33578
	.short	33579
	.short	21
	.short	33580
	.short	85
	.short	33581
	.short	149
	.short	33582
	.short	213
	.short	33583
	.short	277
	.short	33584
	.short	341
	.short	33585
	.short	533
	.short	33586
	.short	33587
	.short	597
	.short	33588
	.short	661
	.short	33589
	.short	725
	.short	33590
	.short	789
	.short	33591
	.short	853
	.short	33592
	.short	20
	.short	33593
	.short	84
	.short	33594
	.short	33595
	.short	148
	.short	33596
	.short	212
	.short	33597
	.short	276
	.short	33598
	.short	340
	.short	33599
	.short	532
	.short	33600
	.short	596
	.short	33601
	.short	33602
	.short	660
	.short	33603
	.short	724
	.short	33604
	.short	788
	.short	33605
	.short	852
	.short	33606
	.short	19
	.short	33607
	.short	83
	.short	33608
	.short	147
	.short	33609
	.short	33610
	.short	211
	.short	33611
	.short	275
	.short	33612
	.short	339
	.short	33613
	.short	531
	.short	33614
	.short	595
	.short	33615
	.short	659
	.short	33616
	.short	723
	.short	33617
	.short	33618
	.short	787
	.short	33619
	.short	851
	.short	33620
	.short	18
	.short	33621
	.short	82
	.short	33622
	.short	146
	.short	33623
	.short	210
	.short	33624
	.short	33625
	.short	274
	.short	33626
	.short	338
	.short	33627
	.short	530
	.short	33628
	.short	594
	.short	33629
	.short	658
	.short	33630
	.short	722
	.short	33631
	.short	786
	.short	33632
	.short	33633
	.short	850
	.short	33634
	.short	17
	.short	33635
	.short	81
	.short	33636
	.short	145
	.short	33637
	.short	209
	.short	33638
	.short	273
	.short	33639
	.short	337
	.short	33640
	.short	33641
	.short	529
	.short	33642
	.short	593
	.short	33643
	.short	657
	.short	33644
	.short	721
	.short	33645
	.short	785
	.short	33646
	.short	849
	.short	33647
	.short	16
	.short	33648
	.short	33649
	.short	80
	.short	33650
	.short	144
	.short	33651
	.short	208
	.short	33652
	.short	272
	.short	33653
	.short	336
	.short	33654
	.short	528
	.short	33655
	.short	33656
	.short	592
	.short	33657
	.short	656
	.short	33658
	.short	720
	.short	33659
	.short	784
	.short	33660
	.short	848
	.short	33661
	.short	15
	.short	33662
	.short	79
	.short	33663
	.short	33664
	.short	143
	.short	33665
	.short	207
	.short	33666
	.short	271
	.short	33667
	.short	335
	.short	33668
	.short	527
	.short	33669
	.short	591
	.short	33670
	.short	655
	.short	33671
	.short	33672
	.short	719
	.short	33673
	.short	783
	.short	33674
	.short	847
	.short	33675
	.short	14
	.short	33676
	.short	78
	.short	33677
	.short	142
	.short	33678
	.short	206
	.short	33679
	.short	33680
	.short	270
	.short	33681
	.short	334
	.short	33682
	.short	526
	.short	33683
	.short	590
	.short	33684
	.short	654
	.short	33685
	.short	718
	.short	33686
	.short	33687
	.short	782
	.short	33688
	.short	846
	.short	33689
	.short	13
	.short	33690
	.short	77
	.short	33691
	.short	141
	.short	33692
	.short	205
	.short	33693
	.short	269
	.short	33694
	.short	33695
	.short	333
	.short	33696
	.short	525
	.short	33697
	.short	589
	.short	33698
	.short	653
	.short	33699
	.short	717
	.short	33700
	.short	781
	.short	33701
	.short	845
	.short	33702
	.short	33703
	.short	12
	.short	33704
	.short	76
	.short	33705
	.short	140
	.short	33706
	.short	204
	.short	33707
	.short	268
	.short	33708
	.short	332
	.short	33709
	.short	33710
	.short	524
	.short	33711
	.short	588
	.short	33712
	.short	652
	.short	33713
	.short	716
	.short	33714
	.short	780
	.short	33715
	.short	844
	.short	33716
	.short	11
	.short	33717
	.short	33718
	.short	75
	.short	33719
	.short	139
	.short	33720
	.short	203
	.short	33721
	.short	267
	.short	33722
	.short	331
	.short	33723
	.short	523
	.short	33724
	.short	587
	.short	33725
	.short	33726
	.short	651
	.short	33727
	.short	715
	.short	33728
	.short	779
	.short	33729
	.short	843
	.short	33730
	.short	10
	.short	33731
	.short	74
	.short	33732
	.short	138
	.short	33733
	.short	33734
	.short	202
	.short	33735
	.short	266
	.short	33736
	.short	330
	.short	33737
	.short	522
	.short	33738
	.short	586
	.short	33739
	.short	650
	.short	33740
	.short	33741
	.short	714
	.short	33742
	.short	778
	.short	33743
	.short	842
	.short	33744
	.short	9
	.short	33745
	.short	73
	.short	33746
	.short	137
	.short	33747
	.short	201
	.short	33748
	.short	33749
	.short	265
	.short	33750
	.short	329
	.short	33751
	.short	521
	.short	33752
	.short	585
	.short	33753
	.short	649
	.short	33754
	.short	713
	.short	33755
	.short	777
	.short	33756
	.short	33757
	.short	841
	.short	33758
	.short	8
	.short	33759
	.short	72
	.short	33760
	.short	136
	.short	33761
	.short	200
	.short	33762
	.short	264
	.short	33763
	.short	328
	.short	33764
	.short	33765
	.short	520
	.short	33766
	.short	584
	.short	33767
	.short	648
	.short	33768
	.short	712
	.short	33769
	.short	776
	.short	33770
	.short	840
	.short	33771
	.short	33772
	.short	7
	.short	33773
	.short	71
	.short	33774
	.short	135
	.short	33775
	.short	199
	.short	33776
	.short	263
	.short	33777
	.short	327
	.short	33778
	.short	519
	.short	33779
	.short	33780
	.short	583
	.short	33781
	.short	647
	.short	33782
	.short	711
	.short	33783
	.short	775
	.short	33784
	.short	839
	.short	33785
	.short	6
	.short	33786
	.short	70
	.short	33787
	.short	33788
	.short	134
	.short	33789
	.short	198
	.short	33790
	.short	262
	.short	33791
	.short	326
	.short	33792
	.short	518
	.short	33793
	.short	582
	.short	33794
	.short	33795
	.short	646
	.short	33796
	.short	710
	.short	33797
	.short	774
	.short	33798
	.short	838
	.short	33799
	.short	5
	.short	33800
	.short	69
	.short	33801
	.short	133
	.short	33802
	.short	33803
	.short	197
	.short	33804
	.short	261
	.short	33805
	.short	325
	.short	33806
	.short	517
	.short	33807
	.short	581
	.short	33808
	.short	645
	.short	33809
	.short	709
	.short	33810
	.short	33811
	.short	773
	.short	33812
	.short	837
	.short	33813
	.short	4
	.short	33814
	.short	68
	.short	33815
	.short	132
	.short	33816
	.short	196
	.short	33817
	.short	260
	.short	33818
	.short	33819
	.short	324
	.short	33820
	.short	516
	.short	33821
	.short	580
	.short	33822
	.short	644
	.short	33823
	.short	708
	.short	33824
	.short	772
	.short	33825
	.short	33826
	.short	836
	.short	33827
	.short	3
	.short	33828
	.short	67
	.short	33829
	.short	131
	.short	33830
	.short	195
	.short	33831
	.short	259
	.short	33832
	.short	323
	.short	33833
	.short	33834
	.short	515
	.short	33835
	.short	579
	.short	33836
	.short	643
	.short	33837
	.short	707
	.short	33838
	.short	771
	.short	33839
	.short	835
	.short	33840
	.short	2
	.short	33841
	.short	33842
	.short	66
	.short	33843
	.short	130
	.short	33844
	.short	194
	.short	33845
	.short	258
	.short	33846
	.short	322
	.short	33847
	.short	514
	.short	33848
	.short	578
	.short	33849
	.short	33850
	.short	642
	.short	33851
	.short	706
	.short	33852
	.short	770
	.short	33853
	.short	834
	.short	33854
	.short	1
	.short	33855
	.short	65
	.short	33856
	.short	33857
	.short	129
	.short	33858
	.short	193
	.short	33859
	.short	257
	.short	33860
	.short	321
	.short	33861
	.short	513
	.short	33862
	.short	577
	.short	33863
	.short	641
	.short	33864
	.short	33865
	.short	705
	.short	33866
	.short	769
	.short	33867
	.short	833
	.short	33868
	.short	0
	.short	33869
	.short	64
	.short	33870
	.short	128
	.short	33871
	.short	192
	.short	33872
	.short	33873
	.short	256
	.short	33874
	.short	320
	.short	33875
	.short	512
	.short	33876
	.short	576
	.short	33877
	.short	640
	.short	33878
	.short	704
	.short	33879
	.short	768
	.short	33880
	.short	33881
	.short	832
	.short	33882
	.short	16384
	.short	33883
	.short	16640
	.short	33884
	.short	16896
	.short	33885
	.short	17152
	.short	33886
	.short	17408
	.short	33887
	.short	33888
	.short	18432
	.short	33889
	.short	18688
	.short	33890
	.short	18944
	.short	33891
	.short	19200
	.short	33892
	.short	19456
	.short	33893
	.short	16400
	.short	33894
	.short	16656
	.short	33895
	.short	33896
	.short	16912
	.short	33897
	.short	17168
	.short	33898
	.short	17424
	.short	33899
	.short	18448
	.short	33900
	.short	18704
	.short	33901
	.short	18960
	.short	33902
	.short	19216
	.short	33903
	.short	33904
	.short	19472
	.short	33905
	.short	16416
	.short	33906
	.short	16672
	.short	33907
	.short	16928
	.short	33908
	.short	17184
	.short	33909
	.short	17440
	.short	33910
	.short	33911
	.short	18464
	.short	33912
	.short	18720
	.short	33913
	.short	18976
	.short	33914
	.short	19232
	.short	33915
	.short	19488
	.short	33916
	.short	16432
	.short	33917
	.short	16688
	.short	33918
	.short	33919
	.short	16944
	.short	33920
	.short	17200
	.short	33921
	.short	17456
	.short	33922
	.short	18480
	.short	33923
	.short	18736
	.short	33924
	.short	18992
	.short	33925
	.short	19248
	.short	33926
	.short	33927
	.short	19504
	.short	33928
	.short	16448
	.short	33929
	.short	16704
	.short	33930
	.short	16960
	.short	33931
	.short	17216
	.short	33932
	.short	17472
	.short	33933
	.short	18496
	.short	33934
	.short	33935
	.short	18752
	.short	33936
	.short	19008
	.short	33937
	.short	19264
	.short	33938
	.short	19520
	.short	33939
	.short	16464
	.short	33940
	.short	16720
	.short	33941
	.short	33942
	.short	16976
	.short	33943
	.short	17232
	.short	33944
	.short	17488
	.short	33945
	.short	18512
	.short	33946
	.short	18768
	.short	33947
	.short	19024
	.short	33948
	.short	19280
	.short	33949
	.short	33950
	.short	19536
	.short	33951
	.short	16480
	.short	33952
	.short	16736
	.short	33953
	.short	16992
	.short	33954
	.short	17248
	.short	33955
	.short	17504
	.short	33956
	.short	18528
	.short	33957
	.short	33958
	.short	18784
	.short	33959
	.short	19040
	.short	33960
	.short	19296
	.short	33961
	.short	19552
	.short	33962
	.short	16496
	.short	33963
	.short	16752
	.short	33964
	.short	17008
	.short	33965
	.short	33966
	.short	17264
	.short	33967
	.short	17520
	.short	33968
	.short	18544
	.short	33969
	.short	18800
	.short	33970
	.short	19056
	.short	33971
	.short	19312
	.short	33972
	.short	33973
	.short	19568
	.short	33974
	.short	16512
	.short	33975
	.short	16768
	.short	33976
	.short	17024
	.short	33977
	.short	17280
	.short	33978
	.short	17536
	.short	33979
	.short	18560
	.short	33980
	.short	33981
	.short	18816
	.short	33982
	.short	19072
	.short	33983
	.short	19328
	.short	33984
	.short	19584
	.short	33985
	.short	16528
	.short	33986
	.short	16784
	.short	33987
	.short	17040
	.short	33988
	.short	33989
	.short	17296
	.short	33990
	.short	17552
	.short	33991
	.short	18576
	.short	33992
	.short	18832
	.short	33993
	.short	19088
	.short	33994
	.short	19344
	.short	33995
	.short	33996
	.short	19600
	.short	33997
	.short	16544
	.short	33998
	.short	16800
	.short	33999
	.short	17056
	.short	34000
	.short	17312
	.short	34001
	.short	17568
	.short	34002
	.short	18592
	.short	34003
	.short	34004
	.short	18848
	.short	34005
	.short	19104
	.short	34006
	.short	19360
	.short	34007
	.short	19616
	.short	34008
	.short	16560
	.short	34009
	.short	16816
	.short	34010
	.short	17072
	.short	34011
	.short	34012
	.short	17328
	.short	34013
	.short	17584
	.short	34014
	.short	18608
	.short	34015
	.short	18864
	.short	34016
	.short	19120
	.short	34017
	.short	19376
	.short	34018
	.short	19632
	.short	34019
	.short	34020
	.short	16576
	.short	34021
	.short	16832
	.short	34022
	.short	17088
	.short	34023
	.short	17344
	.short	34024
	.short	17600
	.short	34025
	.short	18624
	.short	34026
	.short	34027
	.short	18880
	.short	34028
	.short	19136
	.short	34029
	.short	19392
	.short	34030
	.short	19648
	.short	34031
	.short	16592
	.short	34032
	.short	16848
	.short	34033
	.short	17104
	.short	34034
	.short	34035
	.short	17360
	.short	34036
	.short	17616
	.short	34037
	.short	18640
	.short	34038
	.short	18896
	.short	34039
	.short	19152
	.short	34040
	.short	19408
	.short	34041
	.short	19664
	.short	34042
	.short	34043
	.short	16608
	.short	34044
	.short	16864
	.short	34045
	.short	17120
	.short	34046
	.short	17376
	.short	34047
	.short	17632
	.short	34048
	.short	18656
	.short	34049
	.short	18912
	.short	34050
	.short	34051
	.short	19168
	.short	34052
	.short	19424
	.short	34053
	.short	19680
	.short	34054
	.short	16385
	.short	34055
	.short	16641
	.short	34056
	.short	16897
	.short	34057
	.short	34058
	.short	17153
	.short	34059
	.short	17409
	.short	34060
	.short	18433
	.short	34061
	.short	18689
	.short	34062
	.short	18945
	.short	34063
	.short	19201
	.short	34064
	.short	19457
	.short	34065
	.short	34066
	.short	16401
	.short	34067
	.short	16657
	.short	34068
	.short	16913
	.short	34069
	.short	17169
	.short	34070
	.short	17425
	.short	34071
	.short	18449
	.short	34072
	.short	18705
	.short	34073
	.short	34074
	.short	18961
	.short	34075
	.short	19217
	.short	34076
	.short	19473
	.short	34077
	.short	16417
	.short	34078
	.short	16673
	.short	34079
	.short	16929
	.short	34080
	.short	34081
	.short	17185
	.short	34082
	.short	17441
	.short	34083
	.short	18465
	.short	34084
	.short	18721
	.short	34085
	.short	18977
	.short	34086
	.short	19233
	.short	34087
	.short	19489
	.short	34088
	.short	34089
	.short	16433
	.short	34090
	.short	16689
	.short	34091
	.short	16945
	.short	34092
	.short	17201
	.short	34093
	.short	17457
	.short	34094
	.short	18481
	.short	34095
	.short	18737
	.short	34096
	.short	34097
	.short	18993
	.short	34098
	.short	19249
	.short	34099
	.short	19505
	.short	34100
	.short	16449
	.short	34101
	.short	16705
	.short	34102
	.short	16961
	.short	34103
	.short	17217
	.short	34104
	.short	34105
	.short	17473
	.short	34106
	.short	18497
	.short	34107
	.short	18753
	.short	34108
	.short	19009
	.short	34109
	.short	19265
	.short	34110
	.short	19521
	.short	34111
	.short	34112
	.short	16465
	.short	34113
	.short	16721
	.short	34114
	.short	16977
	.short	34115
	.short	17233
	.short	34116
	.short	17489
	.short	34117
	.short	18513
	.short	34118
	.short	18769
	.short	34119
	.short	34120
	.short	19025
	.short	34121
	.short	19281
	.short	34122
	.short	19537
	.short	34123
	.short	16481
	.short	34124
	.short	16737
	.short	34125
	.short	16993
	.short	34126
	.short	17249
	.short	34127
	.short	34128
	.short	17505
	.short	34129
	.short	18529
	.short	34130
	.short	18785
	.short	34131
	.short	19041
	.short	34132
	.short	19297
	.short	34133
	.short	19553
	.short	34134
	.short	16497
	.short	34135
	.short	34136
	.short	16753
	.short	34137
	.short	17009
	.short	34138
	.short	17265
	.short	34139
	.short	17521
	.short	34140
	.short	18545
	.short	34141
	.short	18801
	.short	34142
	.short	34143
	.short	19057
	.short	34144
	.short	19313
	.short	34145
	.short	19569
	.short	34146
	.short	16513
	.short	34147
	.short	16769
	.short	34148
	.short	17025
	.short	34149
	.short	17281
	.short	34150
	.short	34151
	.short	17537
	.short	34152
	.short	18561
	.short	34153
	.short	18817
	.short	34154
	.short	19073
	.short	34155
	.short	19329
	.short	34156
	.short	19585
	.short	34157
	.short	16529
	.short	34158
	.short	34159
	.short	16785
	.short	34160
	.short	17041
	.short	34161
	.short	17297
	.short	34162
	.short	17553
	.short	34163
	.short	18577
	.short	34164
	.short	18833
	.short	34165
	.short	34166
	.short	19089
	.short	34167
	.short	19345
	.short	34168
	.short	19601
	.short	34169
	.short	16545
	.short	34170
	.short	16801
	.short	34171
	.short	17057
	.short	34172
	.short	17313
	.short	34173
	.short	34174
	.short	17569
	.short	34175
	.short	18593
	.short	34176
	.short	18849
	.short	34177
	.short	19105
	.short	34178
	.short	19361
	.short	34179
	.short	19617
	.short	34180
	.short	16386
	.short	34181
	.short	34182
	.short	16642
	.short	34183
	.short	16898
	.short	34184
	.short	17154
	.short	34185
	.short	17410
	.short	34186
	.short	18434
	.short	34187
	.short	18690
	.short	34188
	.short	18946
	.short	34189
	.short	34190
	.short	19202
	.short	34191
	.short	19458
	.short	34192
	.short	16402
	.short	34193
	.short	16658
	.short	34194
	.short	16914
	.short	34195
	.short	17170
	.short	34196
	.short	34197
	.short	17426
	.short	34198
	.short	18450
	.short	34199
	.short	18706
	.short	34200
	.short	18962
	.short	34201
	.short	19218
	.short	34202
	.short	19474
	.short	34203
	.short	16418
	.short	34204
	.short	34205
	.short	16674
	.short	34206
	.short	16930
	.short	34207
	.short	17186
	.short	34208
	.short	17442
	.short	34209
	.short	18466
	.short	34210
	.short	18722
	.short	34211
	.short	18978
	.short	34212
	.short	34213
	.short	19234
	.short	34214
	.short	19490
	.short	34215
	.short	16434
	.short	34216
	.short	16690
	.short	34217
	.short	16946
	.short	34218
	.short	17202
	.short	34219
	.short	17458
	.short	34220
	.short	34221
	.short	18482
	.short	34222
	.short	18738
	.short	34223
	.short	18994
	.short	34224
	.short	19250
	.short	34225
	.short	19506
	.short	34226
	.short	16450
	.short	34227
	.short	34228
	.short	16706
	.short	34229
	.short	16962
	.short	34230
	.short	17218
	.short	34231
	.short	17474
	.short	34232
	.short	18498
	.short	34233
	.short	18754
	.short	34234
	.short	19010
	.short	34235
	.short	34236
	.short	19266
	.short	34237
	.short	19522
	.short	34238
	.short	16466
	.short	34239
	.short	16722
	.short	34240
	.short	16978
	.short	34241
	.short	17234
	.short	34242
	.short	17490
	.short	34243
	.short	34244
	.short	18514
	.short	34245
	.short	18770
	.short	34246
	.short	19026
	.short	34247
	.short	19282
	.short	34248
	.short	19538
	.short	34249
	.short	16482
	.short	34250
	.short	16738
	.short	34251
	.short	34252
	.short	16994
	.short	34253
	.short	17250
	.short	34254
	.short	17506
	.short	34255
	.short	18530
	.short	34256
	.short	18786
	.short	34257
	.short	19042
	.short	34258
	.short	34259
	.short	19298
	.short	34260
	.short	19554
	.short	34261
	.short	16498
	.short	34262
	.short	16754
	.short	34263
	.short	17010
	.short	34264
	.short	17266
	.short	34265
	.short	17522
	.short	34266
	.short	34267
	.short	18546
	.short	34268
	.short	18802
	.short	34269
	.short	19058
	.short	34270
	.short	19314
	.short	34271
	.short	19570
	.short	34272
	.short	16387
	.short	34273
	.short	16643
	.short	34274
	.short	34275
	.short	16899
	.short	34276
	.short	17155
	.short	34277
	.short	17411
	.short	34278
	.short	18435
	.short	34279
	.short	18691
	.short	34280
	.short	18947
	.short	34281
	.short	34282
	.short	19203
	.short	34283
	.short	19459
	.short	34284
	.short	16403
	.short	34285
	.short	16659
	.short	34286
	.short	16915
	.short	34287
	.short	17171
	.short	34288
	.short	17427
	.short	34289
	.short	34290
	.short	18451
	.short	34291
	.short	18707
	.short	34292
	.short	18963
	.short	34293
	.short	19219
	.short	34294
	.short	19475
	.short	34295
	.short	16419
	.short	34296
	.short	16675
	.short	34297
	.short	34298
	.short	16931
	.short	34299
	.short	17187
	.short	34300
	.short	17443
	.short	34301
	.short	18467
	.short	34302
	.short	18723
	.short	34303
	.short	18979
	.short	34304
	.short	19235
	.short	34305
	.short	34306
	.short	19491
	.short	34307
	.short	16435
	.short	34308
	.short	16691
	.short	34309
	.short	16947
	.short	34310
	.short	17203
	.short	34311
	.short	17459
	.short	34312
	.short	34313
	.short	18483
	.short	34314
	.short	18739
	.short	34315
	.short	18995
	.short	34316
	.short	19251
	.short	34317
	.short	19507
	.short	34318
	.short	16451
	.short	34319
	.short	16707
	.short	34320
	.short	34321
	.short	16963
	.short	34322
	.short	17219
	.short	34323
	.short	17475
	.short	34324
	.short	18499
	.short	34325
	.short	18755
	.short	34326
	.short	19011
	.short	34327
	.short	19267
	.short	34328
	.short	34329
	.short	19523
	.short	34330
	.short	16467
	.short	34331
	.short	16723
	.short	34332
	.short	16979
	.short	34333
	.short	17235
	.short	34334
	.short	17491
	.short	34335
	.short	18515
	.short	34336
	.short	34337
	.short	18771
	.short	34338
	.short	19027
	.short	34339
	.short	19283
	.short	34340
	.short	19539
	.short	34341
	.short	16388
	.short	34342
	.short	16644
	.short	34343
	.short	34344
	.short	16900
	.short	34345
	.short	17156
	.short	34346
	.short	17412
	.short	34347
	.short	18436
	.short	34348
	.short	18692
	.short	34349
	.short	18948
	.short	34350
	.short	19204
	.short	34351
	.short	34352
	.short	19460
	.short	34353
	.short	16404
	.short	34354
	.short	16660
	.short	34355
	.short	16916
	.short	34356
	.short	17172
	.short	34357
	.short	17428
	.short	34358
	.short	18452
	.short	34359
	.short	34360
	.short	18708
	.short	34361
	.short	18964
	.short	34362
	.short	19220
	.short	34363
	.short	19476
	.short	34364
	.short	16420
	.short	34365
	.short	16676
	.short	34366
	.short	34367
	.short	16932
	.short	34368
	.short	17188
	.short	34369
	.short	17444
	.short	34370
	.short	18468
	.short	34371
	.short	18724
	.short	34372
	.short	18980
	.short	34373
	.short	19236
	.short	34374
	.short	34375
	.short	19492
	.short	34376
	.short	16436
	.short	34377
	.short	16692
	.short	34378
	.short	16948
	.short	34379
	.short	17204
	.short	34380
	.short	17460
	.short	34381
	.short	18484
	.short	34382
	.short	34383
	.short	18740
	.short	34384
	.short	18996
	.short	34385
	.short	19252
	.short	34386
	.short	19508
	.short	34387
	.short	16389
	.short	34388
	.short	16645
	.short	34389
	.short	16901
	.short	34390
	.short	34391
	.short	17157
	.short	34392
	.short	17413
	.short	34393
	.short	18437
	.short	34394
	.short	18693
	.short	34395
	.short	18949
	.short	34396
	.short	19205
	.short	34397
	.short	34398
	.short	19461
	.short	34399
	.short	16405
	.short	34400
	.short	16661
	.short	34401
	.short	16917
	.short	34402
	.short	17173
	.short	34403
	.short	17429
	.short	34404
	.short	18453
	.short	34405
	.short	34406
	.short	18709
	.short	34407
	.short	18965
	.short	34408
	.short	19221
	.short	34409
	.short	19477
	.short	34410
	.short	16421
	.short	34411
	.short	16677
	.short	34412
	.short	16933
	.short	34413
	.short	34414
	.short	17189
	.short	34415
	.short	17445
	.short	34416
	.short	18469
	.short	34417
	.short	18725
	.short	34418
	.short	18981
	.short	34419
	.short	19237
	.short	34420
	.short	19493
	.short	34421
	.short	34422
	.short	16390
	.short	34423
	.short	16646
	.short	34424
	.short	16902
	.short	34425
	.short	17158
	.short	34426
	.short	17414
	.short	34427
	.short	18438
	.short	34428
	.short	34429
	.short	18694
	.short	34430
	.short	18950
	.short	34431
	.short	19206
	.short	34432
	.short	19462
	.short	34433
	.short	16406
	.short	34434
	.short	16662
	.short	34435
	.short	16918
	.short	34436
	.short	34437
	.short	17174
	.short	34438
	.short	17430
	.short	34439
	.short	18454
	.short	34440
	.short	18710
	.short	34441
	.short	18966
	.short	34442
	.short	19222
	.short	34443
	.short	19478
	.short	34444
	.short	34445
	.short	16391
	.short	34446
	.short	16647
	.short	34447
	.short	16903
	.short	34448
	.short	17159
	.short	34449
	.short	17415
	.short	34450
	.short	18439
	.short	34451
	.short	34452
	.short	18695
	.short	34453
	.short	18951
	.short	34454
	.short	19207
	.short	34455
	.short	19463
	.short	34456
	.short	34457
	.short	34458
	.short	34459
	.short	34460
	.short	34461
	.short	34462
	.short	34463
	.short	34464
	.short	34465
	.short	34466
	.short	34467
	.short	34468
	.short	34469
	.short	34470
	.short	34471
	.short	34472
	.short	34473
	.short	34474
	.short	34475
	.short	34476
	.short	34477
	.short	34478
	.short	34479
	.short	34480
	.short	34481
	.short	34482
	.short	34483
	.short	34484
	.short	34485
	.short	34486
	.short	34487
	.short	34488
	.short	34489
	.short	34490
	.short	34491
	.short	34492
	.short	34493
	.short	34494
	.short	34495
	.short	34496
	.short	34497
	.short	34498
	.short	34499
	.short	34500
	.short	34501
	.short	34502
	.short	34503
	.short	34504
	.short	34505
	.short	34506
	.short	34507
	.short	34508
	.short	34509
	.short	34510
	.short	34511
	.short	34512
	.short	34513
	.short	34514
	.short	34515
	.short	34516
	.short	34517
	.short	34518
	.short	34519
	.short	34520
	.short	34521
	.short	34522
	.short	34523
	.short	34524
	.short	34525
	.short	34526
	.short	34527
	.short	34528
	.short	34529
	.short	34530
	.short	34531
	.short	34532
	.short	34533
	.short	34534
	.short	34535
	.short	34536
	.short	34537
	.short	34538
	.short	34539
	.short	34540
	.short	34541
	.short	34542
	.short	34543
	.short	34544
	.short	34545
	.short	34546
	.short	34547
	.short	34548
	.short	34549
	.short	34550
	.short	34551
	.short	34552
	.short	34553
	.short	34554
	.short	34555
	.short	34556
	.short	34557
	.short	34558
	.short	34559
	.short	34560
	.short	34561
	.short	34562
	.short	34563
	.short	34564
	.short	34565
	.short	34566
	.short	34567
	.short	34568
	.short	34569
	.short	34570
	.short	34571
	.short	34572
	.short	34573
	.short	34574
	.short	34575
	.short	34576
	.short	34577
	.short	34578
	.short	34579
	.short	34580
	.short	34581
	.short	34582
	.short	34583
	.short	34584
	.short	34585
	.short	34586
	.short	34587
	.short	34588
	.short	34589
	.short	34590
	.short	34591
	.short	34592
	.short	34593
	.short	34594
	.short	34595
	.short	34596
	.short	34597
	.short	34598
	.short	34599
	.short	34600
	.short	34601
	.short	34602
	.short	34603
	.short	34604
	.short	34605
	.short	34606
	.short	34607
	.short	34608
	.short	34609
	.short	34610
	.short	34611
	.short	34612
	.short	34613
	.short	34614
	.short	34615
	.short	34616
	.short	34617
	.short	34618
	.short	34619
	.short	34620
	.short	34621
	.short	34622
	.short	34623
	.short	34624
	.short	34625
	.short	34626
	.short	34627
	.short	34628
	.short	34629
	.short	34630
	.short	34631
	.short	34632
	.short	34633
	.short	34634
	.short	34635
	.short	34636
	.short	34637
	.short	34638
	.short	34639
	.short	34640
	.short	34641
	.short	34642
	.short	34643
	.short	34644
	.short	34645
	.short	34646
	.short	34647
	.short	34648
	.short	34649
	.short	34650
	.short	34651
	.short	34652
	.short	34653
	.short	34654
	.short	34655
	.short	34656
	.short	34657
	.short	34658
	.short	34659
	.short	34660
	.short	34661
	.short	34662
	.short	34663
	.short	34664
	.short	34665
	.short	34666
	.short	34667
	.short	34668
	.short	34669
	.short	34670
	.short	34671
	.short	34672
	.short	34673
	.short	34674
	.short	34675
	.short	34676
	.short	34677
	.short	34678
	.short	34679
	.short	34680
	.short	34681
	.short	34682
	.short	34683
	.short	34684
	.short	34685
	.short	34686
	.short	34687
	.short	34688
	.short	34689
	.short	34690
	.short	34691
	.short	34692
	.short	34693
	.short	34694
	.short	34695
	.short	34696
	.short	34697
	.short	34698
	.short	34699
	.short	34700
	.short	34701
	.short	34702
	.short	34703
	.short	34704
	.short	34705
	.short	34706
	.short	34707
	.short	34708
	.short	34709
	.short	34710
	.short	34711
	.short	34712
	.short	34713
	.short	34714
	.short	34715
	.short	34716
	.short	34717
	.short	34718
	.short	34719
	.short	34720
	.short	34721
	.short	34722
	.short	34723
	.short	34724
	.short	34725
	.short	34726
	.short	34727
	.short	34728
	.short	34729
	.short	34730
	.short	34731
	.short	34732
	.short	34733
	.short	34734
	.short	34735
	.short	34736
	.short	34737
	.short	34738
	.short	34739
	.short	34740
	.short	34741
	.short	34742
	.short	34743
	.short	34744
	.short	34745
	.short	34746
	.short	34747
	.short	34748
	.short	34749
	.short	34750
	.short	34751
	.short	34752
	.short	34753
	.short	34754
	.short	34755
	.short	34756
	.short	34757
	.short	34758
	.short	34759
	.short	34760
	.short	34761
	.short	34762
	.short	34763
	.short	34764
	.short	34765
	.short	34766
	.short	34767
	.short	34768
	.short	34769
	.short	34770
	.short	34771
	.short	34772
	.short	34773
	.short	34774
	.short	34775
	.short	34776
	.short	34777
	.short	34778
	.short	34779
	.short	34780
	.short	34781
	.short	34782
	.short	34783
	.short	34784
	.short	34785
	.short	34786
	.short	34787
	.short	34788
	.short	34789
	.short	34790
	.short	34791
	.short	34792
	.short	34793
	.short	34794
	.short	34795
	.short	34796
	.short	34797
	.short	34798
	.short	34799
	.short	34800
	.short	34801
	.short	34802
	.short	34803
	.short	34804
	.short	34805
	.short	34806
	.short	34807
	.short	34808
	.short	34809
	.short	34810
	.short	34811
	.short	34812
	.short	34813
	.short	34814
	.short	34815
	.short	34816
	.short	34817
	.short	34818
	.short	34819
	.short	34820
	.short	34821
	.short	34822
	.short	34823
	.short	34824
	.short	34825
	.short	34826
	.short	34827
	.short	34828
	.short	34829
	.short	34830
	.short	34831
	.short	34832
	.short	34833
	.short	34834
	.short	34835
	.short	34836
	.short	34837
	.short	34838
	.short	34839
	.short	34840
	.short	34841
	.short	34842
	.short	34843
	.short	34844
	.short	34845
	.short	34846
	.short	34847
	.short	34848
	.short	34849
	.short	34850
	.short	34851
	.short	34852
	.short	34853
	.short	34854
	.short	34855
	.short	34856
	.short	34857
	.short	34858
	.short	34859
	.short	34860
	.short	34861
	.short	34862
	.short	34863
	.short	34864
	.short	34865
	.short	34866
	.short	34867
	.short	34868
	.short	34869
	.short	34870
	.short	34871
	.short	34872
	.short	34873
	.short	34874
	.short	34875
	.short	34876
	.short	34877
	.short	34878
	.short	34879
	.short	20657
	.short	20913
	.short	21169
	.short	21425
	.short	21681
	.short	22705
	.short	22961
	.short	23217
	.short	23473
	.short	23729
	.short	20673
	.short	20929
	.short	21185
	.short	21441
	.short	21697
	.short	22721
	.short	22977
	.short	23233
	.short	23489
	.short	23745
	.short	20689
	.short	20945
	.short	21201
	.short	21457
	.short	21713
	.short	22737
	.short	22993
	.short	23249
	.short	23505
	.short	23761
	.short	20610
	.short	20866
	.short	21122
	.short	21378
	.short	21634
	.short	22658
	.short	22914
	.short	23170
	.short	23426
	.short	23682
	.short	20626
	.short	20882
	.short	21138
	.short	21394
	.short	21650
	.short	22674
	.short	22930
	.short	23186
	.short	23442
	.short	23698
	.short	20642
	.short	20898
	.short	21154
	.short	21410
	.short	21666
	.short	22690
	.short	22946
	.short	23202
	.short	23458
	.short	23714
	.short	20579
	.short	20835
	.short	21091
	.short	21347
	.short	21603
	.short	22627
	.short	22883
	.short	23139
	.short	23395
	.short	23651
	.short	20595
	.short	20851
	.short	21107
	.short	21363
	.short	21619
	.short	22643
	.short	22899
	.short	23155
	.short	23411
	.short	23667
	.short	20548
	.short	20804
	.short	21060
	.short	21316
	.short	21572
	.short	22596
	.short	22852
	.short	23108
	.short	23364
	.short	23620
	.short	20564
	.short	20820
	.short	21076
	.short	21332
	.short	21588
	.short	22612
	.short	22868
	.short	23124
	.short	23380
	.short	23636
	.short	20533
	.short	20789
	.short	21045
	.short	21301
	.short	21557
	.short	22581
	.short	22837
	.short	23093
	.short	23349
	.short	23605
	.short	20518
	.short	20774
	.short	21030
	.short	21286
	.short	21542
	.short	22566
	.short	22822
	.short	23078
	.short	23334
	.short	23590
	.short	20503
	.short	20759
	.short	21015
	.short	21271
	.short	21527
	.short	22551
	.short	22807
	.short	23063
	.short	23319
	.short	23575
	.short	20488
	.short	20744
	.short	21000
	.short	21256
	.short	21512
	.short	22536
	.short	22792
	.short	23048
	.short	23304
	.short	23560
	.size	_ZN3attL9ATT_ORDERE, 7596

	.type	__hip_cuid_5ba2c1623d679635,@object
